# diff attention loop B (waves 4-7) spacer after sub-head-0 softmax 24 cycles instead of 32
# baseline (speedup 1.0000x reference)
.LBB0_195:
	v_add_u32_e32 v0, s49, v225
	v_add_u32_e32 v6, v0, v227
	v_add_u32_e32 v7, v0, v228
	ds_read_b128 v[244:247], v6
	ds_read_b128 v[248:251], v6 offset:8192
	ds_read_b128 v[236:239], v7
	ds_read_b128 v[208:211], v7 offset:8192
	v_add_u32_e32 v6, v0, v229
	v_add_u32_e32 v7, v0, v230
	ds_read_b128 v[2:5], v6
	ds_read_b128 v[8:11], v6 offset:8192
	ds_read_b128 v[12:15], v7
	s_xor_b64 s[44:45], s[44:45], -1
	v_add_u32_e32 v6, v0, v226
	s_waitcnt lgkmcnt(6)
	v_mfma_f32_32x32x16_bf16 v[144:159], v[244:247], v[176:179], v[144:159]
	ds_read_b128 v[244:247], v7 offset:8192
	s_waitcnt lgkmcnt(6)
	v_mfma_f32_32x32x16_bf16 v[160:175], v[248:251], v[176:179], v[160:175]
	s_waitcnt lgkmcnt(5)
	v_mfma_f32_32x32x16_bf16 v[144:159], v[236:239], v[180:183], v[144:159]
	ds_read_b128 v[248:251], v6
	ds_read_b128 v[236:239], v6 offset:8192
	s_waitcnt lgkmcnt(6)
	v_mfma_f32_32x32x16_bf16 v[160:175], v[208:211], v[180:183], v[160:175]
	v_add_u32_e32 v7, v0, v231
	s_waitcnt lgkmcnt(5)
	v_mfma_f32_32x32x16_bf16 v[144:159], v[2:5], v[184:187], v[144:159]
	s_waitcnt lgkmcnt(4)
	v_mfma_f32_32x32x16_bf16 v[160:175], v[8:11], v[184:187], v[160:175]
	s_waitcnt lgkmcnt(3)
	v_mfma_f32_32x32x16_bf16 v[144:159], v[12:15], v[188:191], v[144:159]
	s_waitcnt lgkmcnt(2)
	v_mfma_f32_32x32x16_bf16 v[160:175], v[244:247], v[188:191], v[160:175]
	ds_read_b128 v[244:247], v7
	s_nop 9
	v_exp_f32_e32 v6, v144
	v_exp_f32_e32 v3, v145
	v_exp_f32_e32 v10, v148
	v_exp_f32_e32 v11, v149
	v_exp_f32_e32 v12, v150
	v_exp_f32_e32 v148, v152
	v_exp_f32_e32 v150, v153
	v_exp_f32_e32 v156, v156
	v_exp_f32_e32 v157, v157
	v_exp_f32_e32 v5, v146
	v_exp_f32_e32 v152, v154
	v_exp_f32_e32 v158, v158
	v_exp_f32_e32 v8, v147
	v_exp_f32_e32 v13, v151
	v_exp_f32_e32 v154, v155
	v_exp_f32_e32 v159, v159
	v_exp_f32_e32 v2, v160
	v_exp_f32_e32 v144, v164
	v_exp_f32_e32 v149, v168
	v_exp_f32_e32 v160, v172
	v_exp_f32_e32 v4, v161
	v_exp_f32_e32 v145, v165
	v_exp_f32_e32 v151, v169
	v_exp_f32_e32 v161, v173
	v_add_f32_e32 v14, v6, v3
	v_add_f32_e32 v15, v10, v11
	v_add_f32_e32 v164, v148, v150
	v_add_f32_e32 v165, v156, v157
	v_exp_f32_e32 v7, v162
	v_exp_f32_e32 v146, v166
	v_exp_f32_e32 v153, v170
	v_exp_f32_e32 v162, v174
	v_add_f32_e32 v14, v5, v14
	v_add_f32_e32 v15, v12, v15
	v_add_f32_e32 v164, v152, v164
	v_add_f32_e32 v165, v158, v165
	v_exp_f32_e32 v9, v163
	v_exp_f32_e32 v147, v167
	v_exp_f32_e32 v155, v171
	v_exp_f32_e32 v163, v175
	v_add_f32_e32 v14, v8, v14
	v_add_f32_e32 v15, v13, v15
	v_add_f32_e32 v164, v154, v164
	v_add_f32_e32 v165, v159, v165
	v_add_f32_e32 v14, v2, v14
	v_add_f32_e32 v15, v144, v15
	v_add_f32_e32 v164, v149, v164
	v_add_f32_e32 v165, v160, v165
	v_add_f32_e32 v14, v4, v14
	v_add_f32_e32 v15, v145, v15
	v_add_f32_e32 v164, v151, v164
	v_add_f32_e32 v165, v161, v165
	v_add_f32_e32 v14, v7, v14
	v_add_f32_e32 v15, v146, v15
	v_add_f32_e32 v164, v153, v164
	v_add_f32_e32 v165, v162, v165
	v_add_f32_e32 v14, v9, v14
	v_add_f32_e32 v15, v147, v15
	v_add_f32_e32 v164, v155, v164
	v_add_f32_e32 v165, v163, v165
	v_add_f32_e32 v14, v14, v15
	v_add_f32_e32 v15, v164, v165
	v_add_f32_e32 v14, v14, v15
	v_mov_b32_e32 v15, v14
	v_cvt_pk_bf16_f32 v208, v6, v3
	v_cvt_pk_bf16_f32 v209, v5, v8
	v_cvt_pk_bf16_f32 v210, v10, v11
	v_cvt_pk_bf16_f32 v211, v12, v13
	v_cvt_pk_bf16_f32 v10, v148, v150
	v_cvt_pk_bf16_f32 v11, v152, v154
	v_cvt_pk_bf16_f32 v12, v156, v157
	v_cvt_pk_bf16_f32 v13, v158, v159
	v_cvt_pk_bf16_f32 v6, v2, v4
	v_cvt_pk_bf16_f32 v7, v7, v9
	v_cvt_pk_bf16_f32 v8, v144, v145
	v_cvt_pk_bf16_f32 v9, v146, v147
	v_cvt_pk_bf16_f32 v2, v149, v151
	v_cvt_pk_bf16_f32 v3, v153, v155
	v_cvt_pk_bf16_f32 v4, v160, v161
	v_cvt_pk_bf16_f32 v5, v162, v163
	v_permlane32_swap_b32_e32 v14, v15
	v_permlane32_swap_b32_e32 v208, v210
	v_permlane32_swap_b32_e32 v209, v211
	v_permlane32_swap_b32_e32 v10, v12
	v_permlane32_swap_b32_e32 v11, v13
	v_permlane32_swap_b32_e32 v6, v8
	v_permlane32_swap_b32_e32 v7, v9
	v_permlane32_swap_b32_e32 v2, v4
	v_permlane32_swap_b32_e32 v3, v5
	s_nop 15
	s_nop 7
	s_andn2_b64 vcc, exec, s[44:45]
	s_cbranch_vccnz .Lz_l1s1
	s_andn2_b64 vcc, exec, s[42:43]
	s_mov_b64 s[42:43], -1
	s_cbranch_vccnz .LBB0_198
	v_add_u32_e32 v144, 0x21780, v212
	v_add_u32_e32 v146, 0x21708, v212
	v_add_u32_e32 v147, 0x21788, v212
	v_add_u32_e32 v148, 0x21720, v212
	v_add_u32_e32 v149, 0x217a0, v212
	v_add_u32_e32 v150, 0x21728, v212
	v_add_u32_e32 v151, 0x217a8, v212
	v_add_u32_e32 v152, 0x21740, v212
	v_add_u32_e32 v153, 0x217c0, v212
	v_add_u32_e32 v154, 0x21748, v212
	v_add_u32_e32 v155, 0x217c8, v212
	v_add_u32_e32 v156, 0x21760, v212
	v_add_u32_e32 v157, 0x217e0, v212
	v_add_u32_e32 v158, 0x21768, v212
	v_add_u32_e32 v159, 0x217e8, v212
	ds_read2_b32 v[160:161], v213 offset1:1
	ds_read2_b32 v[144:145], v144 offset1:1
	ds_read2_b32 v[162:163], v146 offset1:1
	ds_read2_b32 v[146:147], v147 offset1:1
	ds_read2_b32 v[164:165], v148 offset1:1
	ds_read2_b32 v[148:149], v149 offset1:1
	ds_read2_b32 v[166:167], v150 offset1:1
	ds_read2_b32 v[150:151], v151 offset1:1
	ds_read2_b32 v[168:169], v152 offset1:1
	ds_read2_b32 v[152:153], v153 offset1:1
	ds_read2_b32 v[170:171], v154 offset1:1
	ds_read2_b32 v[154:155], v155 offset1:1
	ds_read2_b32 v[172:173], v156 offset1:1
	ds_read2_b32 v[156:157], v157 offset1:1
	ds_read2_b32 v[174:175], v158 offset1:1
	ds_read2_b32 v[158:159], v159 offset1:1
	s_mov_b64 s[42:43], 0
